# sc1 write-through on sort2's 16B tinfo/tblk stores
# speedup vs baseline: 1.3200x; 1.0027x over previous
.LBB1_47:
	s_or_b64 exec, exec, s[36:37]
	v_add_u32_e32 v2, v3, v2
	v_add_u32_e32 v2, v2, v4
	v_add_u32_e32 v4, v2, v5
	s_waitcnt lgkmcnt(0)
	s_barrier
	s_and_saveexec_b64 s[22:23], s[8:9]
	s_cbranch_execz .LBB1_55
	s_mov_b32 s8, 0xc350
	v_cmp_gt_i32_e64 s[8:9], s8, v8
	v_mov_b32_e32 v2, 0
	s_and_saveexec_b64 s[24:25], s[8:9]
	s_cbranch_execz .LBB1_54
	v_lshlrev_b32_e32 v2, 2, v6
	ds_read_b32 v2, v2 offset:21504
	s_cmpk_eq_i32 s2, 0xc3
	s_cselect_b32 s33, 10, 32
	s_lshr_b32 s8, s33, 1
	s_waitcnt lgkmcnt(0)
	v_add_u32_e32 v2, v2, v15
	v_ashrrev_i32_e32 v3, 3, v2
	v_and_b32_e32 v5, 7, v2
	v_cmp_le_i32_e64 s[8:9], s8, v3
	s_and_saveexec_b64 s[36:37], s[8:9]
	s_xor_b64 s[8:9], exec, s[36:37]
	v_not_b32_e32 v2, v3
	v_add_lshl_u32 v2, s33, v2, 4
	v_or3_b32 v2, v2, v5, 8
	s_andn2_saveexec_b64 s[8:9], s[8:9]
	v_lshl_or_b32 v2, v3, 4, v5
	s_or_b64 exec, exec, s[8:9]
	v_add_u32_e32 v6, v28, v4
	v_add_u32_e32 v28, s3, v2
	v_ashrrev_i32_e32 v29, 31, v28
	v_lshl_add_u64 v[28:29], v[28:29], 4, s[28:29]
	v_mov_b32_e32 v9, 0
	global_store_dwordx4 v[28:29], v[6:9], off sc1

.LBB1_102:
	s_or_b64 exec, exec, s[4:5]
	s_waitcnt lgkmcnt(0)
	s_barrier
	ds_read_b128 v[2:5], v1
	s_ashr_i32 s3, s2, 31
	s_lshl_b64 s[4:5], s[2:3], 14
	s_add_u32 s4, s26, s4
	s_addc_u32 s5, s27, s5
	s_waitcnt lgkmcnt(0)
	global_store_dwordx4 v1, v[2:5], s[4:5] sc1
	s_mov_b64 s[4:5], 0
